# P8 cached epilogue no longer waits vmcnt(0) (next tile's LDS-DMA prefetch stays in flight under the epilogue); bias global-load path waits on its own
# speedup vs baseline: 1.0167x; 1.0064x over previous
.LBB0_1744:
	s_ashr_i32 s15, s24, 5
	s_cmp_lg_u32 s15, s33
	s_mov_b64 s[26:27], -1
	s_cbranch_scc0 .LBB0_1746
	s_mul_i32 s26, s15, 0x1600
	s_ashr_i32 s27, s26, 31
	s_lshl_b64 s[26:27], s[26:27], 2
	s_add_u32 s15, s44, s26
	s_addc_u32 s17, s45, s27
	s_lshl_b32 s26, s22, 8
	s_ashr_i32 s27, s26, 31
	s_lshl_b64 s[26:27], s[26:27], 2
	s_add_u32 s26, s15, s26
	s_addc_u32 s27, s17, s27
	v_lshlrev_b32_e32 v62, 2, v156
	global_load_dwordx4 v[74:77], v62, s[26:27] offset:16
	global_load_dwordx4 v[78:81], v62, s[26:27]
	global_load_dwordx4 v[58:61], v62, s[26:27] offset:528
	s_nop 0
	global_load_dwordx4 v[62:65], v62, s[26:27] offset:512
	s_waitcnt vmcnt(0)
	s_cbranch_execz .LBB0_1747
	s_branch .LBB0_1748

.LBB0_1747:
	v_lshl_add_u32 v58, s22, 10, v170
	ds_read_b128 v[78:81], v58
	ds_read_b128 v[74:77], v58 offset:16
	ds_read_b128 v[62:65], v58 offset:512
	ds_read_b128 v[58:61], v58 offset:528

.Lp8fast:
	ds_read_b32 v190, v176 offset:704
	ds_read_b32 v188, v176 offset:640
	ds_read_b32 v186, v176 offset:576
	ds_read_b32 v184, v176 offset:512
	ds_read_b32 v182, v176 offset:192
	ds_read_b32 v180, v176 offset:128
	ds_read_b32 v178, v176 offset:64
	ds_read_b32 v176, v176
	s_lshl_b32 s22, s22, 7
	s_ashr_i32 s23, s22, 31
	s_mov_b32 s26, 0xbfb8aa3b
	v_mov_b64_e32 v[218:219], s[8:9]
	v_mad_u64_u32 v[218:219], s[24:25], v166, s53, v[218:219]
	v_mov_b32_e32 v220, v219
	v_mad_u64_u32 v[220:221], s[24:25], v167, s53, v[220:221]
	v_mov_b32_e32 v219, v220
	v_lshl_add_u64 v[218:219], s[22:23], 1, v[218:219]
	v_lshl_add_u64 v[218:219], v[218:219], 0, v[154:155]
	s_waitcnt lgkmcnt(0)
	v_pk_fma_f32 v[142:143], v[142:143], v[176:177], v[78:79] op_sel_hi:[1,0,1]
	v_pk_fma_f32 v[144:145], v[144:145], v[176:177], v[80:81] op_sel_hi:[1,0,1]
	v_pk_fma_f32 v[138:139], v[138:139], v[176:177], v[74:75] op_sel_hi:[1,0,1]
	v_pk_fma_f32 v[140:141], v[140:141], v[176:177], v[76:77] op_sel_hi:[1,0,1]
	v_pk_fma_f32 v[134:135], v[134:135], v[176:177], v[62:63] op_sel_hi:[1,0,1]
	v_pk_fma_f32 v[136:137], v[136:137], v[176:177], v[64:65] op_sel_hi:[1,0,1]
	v_pk_fma_f32 v[130:131], v[130:131], v[176:177], v[58:59] op_sel_hi:[1,0,1]
	v_pk_fma_f32 v[132:133], v[132:133], v[176:177], v[60:61] op_sel_hi:[1,0,1]
	v_pk_mul_f32 v[192:193], v[138:139], s[26:27] op_sel_hi:[1,0]
	v_pk_mul_f32 v[194:195], v[140:141], s[26:27] op_sel_hi:[1,0]
	v_pk_mul_f32 v[196:197], v[142:143], s[26:27] op_sel_hi:[1,0]
	v_pk_mul_f32 v[198:199], v[144:145], s[26:27] op_sel_hi:[1,0]
	v_exp_f32_e32 v192, v192
	v_exp_f32_e32 v193, v193
	v_exp_f32_e32 v194, v194
	v_exp_f32_e32 v195, v195
	v_exp_f32_e32 v196, v196
	v_exp_f32_e32 v197, v197
	v_exp_f32_e32 v198, v198
	v_exp_f32_e32 v199, v199
	v_add_f32_e32 v192, 1.0, v192
	v_add_f32_e32 v193, 1.0, v193
	v_add_f32_e32 v194, 1.0, v194
	v_add_f32_e32 v195, 1.0, v195
	v_add_f32_e32 v196, 1.0, v196
	v_add_f32_e32 v197, 1.0, v197
	v_add_f32_e32 v198, 1.0, v198
	v_add_f32_e32 v199, 1.0, v199
	v_rcp_f32_e32 v192, v192
	v_rcp_f32_e32 v193, v193
	v_rcp_f32_e32 v194, v194
	v_rcp_f32_e32 v195, v195
	v_rcp_f32_e32 v196, v196
	v_rcp_f32_e32 v197, v197
	v_rcp_f32_e32 v198, v198
	v_rcp_f32_e32 v199, v199
	v_pk_mul_f32 v[192:193], v[138:139], v[192:193]
	v_pk_mul_f32 v[194:195], v[140:141], v[194:195]
	v_pk_mul_f32 v[196:197], v[142:143], v[196:197]
	v_pk_mul_f32 v[198:199], v[144:145], v[198:199]
	v_pk_mul_f32 v[202:203], v[192:193], v[130:131]
	v_pk_mul_f32 v[204:205], v[194:195], v[132:133]
	v_pk_mul_f32 v[206:207], v[196:197], v[134:135]
	v_pk_mul_f32 v[208:209], v[198:199], v[136:137]
	v_cvt_pk_bf16_f32 v210, v206, v207
	v_cvt_pk_bf16_f32 v211, v208, v209
	v_cvt_pk_bf16_f32 v212, v202, v203
	v_cvt_pk_bf16_f32 v213, v204, v205
	global_store_dwordx4 v[218:219], v[210:213], off
	v_add_co_u32_e32 v218, vcc, 0x16000, v218
	s_nop 1
	v_addc_co_u32_e32 v219, vcc, 0, v219, vcc
	v_pk_fma_f32 v[126:127], v[126:127], v[178:179], v[78:79] op_sel_hi:[1,0,1]
	v_pk_fma_f32 v[128:129], v[128:129], v[178:179], v[80:81] op_sel_hi:[1,0,1]
	v_pk_fma_f32 v[122:123], v[122:123], v[178:179], v[74:75] op_sel_hi:[1,0,1]
	v_pk_fma_f32 v[124:125], v[124:125], v[178:179], v[76:77] op_sel_hi:[1,0,1]
	v_pk_fma_f32 v[118:119], v[118:119], v[178:179], v[62:63] op_sel_hi:[1,0,1]
	v_pk_fma_f32 v[120:121], v[120:121], v[178:179], v[64:65] op_sel_hi:[1,0,1]
	v_pk_fma_f32 v[114:115], v[114:115], v[178:179], v[58:59] op_sel_hi:[1,0,1]
	v_pk_fma_f32 v[116:117], v[116:117], v[178:179], v[60:61] op_sel_hi:[1,0,1]
	v_pk_mul_f32 v[192:193], v[122:123], s[26:27] op_sel_hi:[1,0]
	v_pk_mul_f32 v[194:195], v[124:125], s[26:27] op_sel_hi:[1,0]
	v_pk_mul_f32 v[196:197], v[126:127], s[26:27] op_sel_hi:[1,0]
	v_pk_mul_f32 v[198:199], v[128:129], s[26:27] op_sel_hi:[1,0]
	v_exp_f32_e32 v192, v192
	v_exp_f32_e32 v193, v193
	v_exp_f32_e32 v194, v194
	v_exp_f32_e32 v195, v195
	v_exp_f32_e32 v196, v196
	v_exp_f32_e32 v197, v197
	v_exp_f32_e32 v198, v198
	v_exp_f32_e32 v199, v199
	v_add_f32_e32 v192, 1.0, v192
	v_add_f32_e32 v193, 1.0, v193
	v_add_f32_e32 v194, 1.0, v194
	v_add_f32_e32 v195, 1.0, v195
	v_add_f32_e32 v196, 1.0, v196
	v_add_f32_e32 v197, 1.0, v197
	v_add_f32_e32 v198, 1.0, v198
	v_add_f32_e32 v199, 1.0, v199
	v_rcp_f32_e32 v192, v192
	v_rcp_f32_e32 v193, v193
	v_rcp_f32_e32 v194, v194
	v_rcp_f32_e32 v195, v195
	v_rcp_f32_e32 v196, v196
	v_rcp_f32_e32 v197, v197
	v_rcp_f32_e32 v198, v198
	v_rcp_f32_e32 v199, v199
	v_pk_mul_f32 v[192:193], v[122:123], v[192:193]
	v_pk_mul_f32 v[194:195], v[124:125], v[194:195]
	v_pk_mul_f32 v[196:197], v[126:127], v[196:197]
	v_pk_mul_f32 v[198:199], v[128:129], v[198:199]
	v_pk_mul_f32 v[202:203], v[192:193], v[114:115]
	v_pk_mul_f32 v[204:205], v[194:195], v[116:117]
	v_pk_mul_f32 v[206:207], v[196:197], v[118:119]
	v_pk_mul_f32 v[208:209], v[198:199], v[120:121]
	v_cvt_pk_bf16_f32 v210, v206, v207
	v_cvt_pk_bf16_f32 v211, v208, v209
	v_cvt_pk_bf16_f32 v212, v202, v203
	v_cvt_pk_bf16_f32 v213, v204, v205
	global_store_dwordx4 v[218:219], v[210:213], off
	v_add_co_u32_e32 v218, vcc, 0x16000, v218
	s_nop 1
	v_addc_co_u32_e32 v219, vcc, 0, v219, vcc
	v_pk_fma_f32 v[110:111], v[110:111], v[180:181], v[78:79] op_sel_hi:[1,0,1]
	v_pk_fma_f32 v[112:113], v[112:113], v[180:181], v[80:81] op_sel_hi:[1,0,1]
	v_pk_fma_f32 v[106:107], v[106:107], v[180:181], v[74:75] op_sel_hi:[1,0,1]
	v_pk_fma_f32 v[108:109], v[108:109], v[180:181], v[76:77] op_sel_hi:[1,0,1]
	v_pk_fma_f32 v[102:103], v[102:103], v[180:181], v[62:63] op_sel_hi:[1,0,1]
	v_pk_fma_f32 v[104:105], v[104:105], v[180:181], v[64:65] op_sel_hi:[1,0,1]
	v_pk_fma_f32 v[98:99], v[98:99], v[180:181], v[58:59] op_sel_hi:[1,0,1]
	v_pk_fma_f32 v[100:101], v[100:101], v[180:181], v[60:61] op_sel_hi:[1,0,1]
	v_pk_mul_f32 v[192:193], v[106:107], s[26:27] op_sel_hi:[1,0]
	v_pk_mul_f32 v[194:195], v[108:109], s[26:27] op_sel_hi:[1,0]
	v_pk_mul_f32 v[196:197], v[110:111], s[26:27] op_sel_hi:[1,0]
	v_pk_mul_f32 v[198:199], v[112:113], s[26:27] op_sel_hi:[1,0]
	v_exp_f32_e32 v192, v192
	v_exp_f32_e32 v193, v193
	v_exp_f32_e32 v194, v194
	v_exp_f32_e32 v195, v195
	v_exp_f32_e32 v196, v196
	v_exp_f32_e32 v197, v197
	v_exp_f32_e32 v198, v198
	v_exp_f32_e32 v199, v199
	v_add_f32_e32 v192, 1.0, v192
	v_add_f32_e32 v193, 1.0, v193
	v_add_f32_e32 v194, 1.0, v194
	v_add_f32_e32 v195, 1.0, v195
	v_add_f32_e32 v196, 1.0, v196
	v_add_f32_e32 v197, 1.0, v197
	v_add_f32_e32 v198, 1.0, v198
	v_add_f32_e32 v199, 1.0, v199
	v_rcp_f32_e32 v192, v192
	v_rcp_f32_e32 v193, v193
	v_rcp_f32_e32 v194, v194
	v_rcp_f32_e32 v195, v195
	v_rcp_f32_e32 v196, v196
	v_rcp_f32_e32 v197, v197
	v_rcp_f32_e32 v198, v198
	v_rcp_f32_e32 v199, v199
	v_pk_mul_f32 v[192:193], v[106:107], v[192:193]
	v_pk_mul_f32 v[194:195], v[108:109], v[194:195]
	v_pk_mul_f32 v[196:197], v[110:111], v[196:197]
	v_pk_mul_f32 v[198:199], v[112:113], v[198:199]
	v_pk_mul_f32 v[202:203], v[192:193], v[98:99]
	v_pk_mul_f32 v[204:205], v[194:195], v[100:101]
	v_pk_mul_f32 v[206:207], v[196:197], v[102:103]
	v_pk_mul_f32 v[208:209], v[198:199], v[104:105]
	v_cvt_pk_bf16_f32 v210, v206, v207
	v_cvt_pk_bf16_f32 v211, v208, v209
	v_cvt_pk_bf16_f32 v212, v202, v203
	v_cvt_pk_bf16_f32 v213, v204, v205
	global_store_dwordx4 v[218:219], v[210:213], off
	v_add_co_u32_e32 v218, vcc, 0x16000, v218
	s_nop 1
	v_addc_co_u32_e32 v219, vcc, 0, v219, vcc
	v_pk_fma_f32 v[94:95], v[94:95], v[182:183], v[78:79] op_sel_hi:[1,0,1]
	v_pk_fma_f32 v[96:97], v[96:97], v[182:183], v[80:81] op_sel_hi:[1,0,1]
	v_pk_fma_f32 v[90:91], v[90:91], v[182:183], v[74:75] op_sel_hi:[1,0,1]
	v_pk_fma_f32 v[92:93], v[92:93], v[182:183], v[76:77] op_sel_hi:[1,0,1]
	v_pk_fma_f32 v[86:87], v[86:87], v[182:183], v[62:63] op_sel_hi:[1,0,1]
	v_pk_fma_f32 v[88:89], v[88:89], v[182:183], v[64:65] op_sel_hi:[1,0,1]
	v_pk_fma_f32 v[82:83], v[82:83], v[182:183], v[58:59] op_sel_hi:[1,0,1]
	v_pk_fma_f32 v[84:85], v[84:85], v[182:183], v[60:61] op_sel_hi:[1,0,1]
	v_pk_mul_f32 v[192:193], v[90:91], s[26:27] op_sel_hi:[1,0]
	v_pk_mul_f32 v[194:195], v[92:93], s[26:27] op_sel_hi:[1,0]
	v_pk_mul_f32 v[196:197], v[94:95], s[26:27] op_sel_hi:[1,0]
	v_pk_mul_f32 v[198:199], v[96:97], s[26:27] op_sel_hi:[1,0]
	v_exp_f32_e32 v192, v192
	v_exp_f32_e32 v193, v193
	v_exp_f32_e32 v194, v194
	v_exp_f32_e32 v195, v195
	v_exp_f32_e32 v196, v196
	v_exp_f32_e32 v197, v197
	v_exp_f32_e32 v198, v198
	v_exp_f32_e32 v199, v199
	v_add_f32_e32 v192, 1.0, v192
	v_add_f32_e32 v193, 1.0, v193
	v_add_f32_e32 v194, 1.0, v194
	v_add_f32_e32 v195, 1.0, v195
	v_add_f32_e32 v196, 1.0, v196
	v_add_f32_e32 v197, 1.0, v197
	v_add_f32_e32 v198, 1.0, v198
	v_add_f32_e32 v199, 1.0, v199
	v_rcp_f32_e32 v192, v192
	v_rcp_f32_e32 v193, v193
	v_rcp_f32_e32 v194, v194
	v_rcp_f32_e32 v195, v195
	v_rcp_f32_e32 v196, v196
	v_rcp_f32_e32 v197, v197
	v_rcp_f32_e32 v198, v198
	v_rcp_f32_e32 v199, v199
	v_pk_mul_f32 v[192:193], v[90:91], v[192:193]
	v_pk_mul_f32 v[194:195], v[92:93], v[194:195]
	v_pk_mul_f32 v[196:197], v[94:95], v[196:197]
	v_pk_mul_f32 v[198:199], v[96:97], v[198:199]
	v_pk_mul_f32 v[202:203], v[192:193], v[82:83]
	v_pk_mul_f32 v[204:205], v[194:195], v[84:85]
	v_pk_mul_f32 v[206:207], v[196:197], v[86:87]
	v_pk_mul_f32 v[208:209], v[198:199], v[88:89]
	v_cvt_pk_bf16_f32 v210, v206, v207
	v_cvt_pk_bf16_f32 v211, v208, v209
	v_cvt_pk_bf16_f32 v212, v202, v203
	v_cvt_pk_bf16_f32 v213, v204, v205
	global_store_dwordx4 v[218:219], v[210:213], off
	v_add_co_u32_e32 v218, vcc, 0x6e000, v218
	s_nop 1
	v_addc_co_u32_e32 v219, vcc, 0, v219, vcc
	v_pk_fma_f32 v[70:71], v[70:71], v[184:185], v[78:79] op_sel_hi:[1,0,1]
	v_pk_fma_f32 v[72:73], v[72:73], v[184:185], v[80:81] op_sel_hi:[1,0,1]
	v_pk_fma_f32 v[66:67], v[66:67], v[184:185], v[74:75] op_sel_hi:[1,0,1]
	v_pk_fma_f32 v[68:69], v[68:69], v[184:185], v[76:77] op_sel_hi:[1,0,1]
	v_pk_fma_f32 v[54:55], v[54:55], v[184:185], v[62:63] op_sel_hi:[1,0,1]
	v_pk_fma_f32 v[56:57], v[56:57], v[184:185], v[64:65] op_sel_hi:[1,0,1]
	v_pk_fma_f32 v[50:51], v[50:51], v[184:185], v[58:59] op_sel_hi:[1,0,1]
	v_pk_fma_f32 v[52:53], v[52:53], v[184:185], v[60:61] op_sel_hi:[1,0,1]
	v_pk_mul_f32 v[192:193], v[66:67], s[26:27] op_sel_hi:[1,0]
	v_pk_mul_f32 v[194:195], v[68:69], s[26:27] op_sel_hi:[1,0]
	v_pk_mul_f32 v[196:197], v[70:71], s[26:27] op_sel_hi:[1,0]
	v_pk_mul_f32 v[198:199], v[72:73], s[26:27] op_sel_hi:[1,0]
	v_exp_f32_e32 v192, v192
	v_exp_f32_e32 v193, v193
	v_exp_f32_e32 v194, v194
	v_exp_f32_e32 v195, v195
	v_exp_f32_e32 v196, v196
	v_exp_f32_e32 v197, v197
	v_exp_f32_e32 v198, v198
	v_exp_f32_e32 v199, v199
	v_add_f32_e32 v192, 1.0, v192
	v_add_f32_e32 v193, 1.0, v193
	v_add_f32_e32 v194, 1.0, v194
	v_add_f32_e32 v195, 1.0, v195
	v_add_f32_e32 v196, 1.0, v196
	v_add_f32_e32 v197, 1.0, v197
	v_add_f32_e32 v198, 1.0, v198
	v_add_f32_e32 v199, 1.0, v199
	v_rcp_f32_e32 v192, v192
	v_rcp_f32_e32 v193, v193
	v_rcp_f32_e32 v194, v194
	v_rcp_f32_e32 v195, v195
	v_rcp_f32_e32 v196, v196
	v_rcp_f32_e32 v197, v197
	v_rcp_f32_e32 v198, v198
	v_rcp_f32_e32 v199, v199
	v_pk_mul_f32 v[192:193], v[66:67], v[192:193]
	v_pk_mul_f32 v[194:195], v[68:69], v[194:195]
	v_pk_mul_f32 v[196:197], v[70:71], v[196:197]
	v_pk_mul_f32 v[198:199], v[72:73], v[198:199]
	v_pk_mul_f32 v[202:203], v[192:193], v[50:51]
	v_pk_mul_f32 v[204:205], v[194:195], v[52:53]
	v_pk_mul_f32 v[206:207], v[196:197], v[54:55]
	v_pk_mul_f32 v[208:209], v[198:199], v[56:57]
	v_cvt_pk_bf16_f32 v210, v206, v207
	v_cvt_pk_bf16_f32 v211, v208, v209
	v_cvt_pk_bf16_f32 v212, v202, v203
	v_cvt_pk_bf16_f32 v213, v204, v205
	global_store_dwordx4 v[218:219], v[210:213], off
	v_add_co_u32_e32 v218, vcc, 0x16000, v218
	s_nop 1
	v_addc_co_u32_e32 v219, vcc, 0, v219, vcc
	v_pk_fma_f32 v[46:47], v[46:47], v[186:187], v[78:79] op_sel_hi:[1,0,1]
	v_pk_fma_f32 v[48:49], v[48:49], v[186:187], v[80:81] op_sel_hi:[1,0,1]
	v_pk_fma_f32 v[42:43], v[42:43], v[186:187], v[74:75] op_sel_hi:[1,0,1]
	v_pk_fma_f32 v[44:45], v[44:45], v[186:187], v[76:77] op_sel_hi:[1,0,1]
	v_pk_fma_f32 v[38:39], v[38:39], v[186:187], v[62:63] op_sel_hi:[1,0,1]
	v_pk_fma_f32 v[40:41], v[40:41], v[186:187], v[64:65] op_sel_hi:[1,0,1]
	v_pk_fma_f32 v[34:35], v[34:35], v[186:187], v[58:59] op_sel_hi:[1,0,1]
	v_pk_fma_f32 v[36:37], v[36:37], v[186:187], v[60:61] op_sel_hi:[1,0,1]
	v_pk_mul_f32 v[192:193], v[42:43], s[26:27] op_sel_hi:[1,0]
	v_pk_mul_f32 v[194:195], v[44:45], s[26:27] op_sel_hi:[1,0]
	v_pk_mul_f32 v[196:197], v[46:47], s[26:27] op_sel_hi:[1,0]
	v_pk_mul_f32 v[198:199], v[48:49], s[26:27] op_sel_hi:[1,0]
	v_exp_f32_e32 v192, v192
	v_exp_f32_e32 v193, v193
	v_exp_f32_e32 v194, v194
	v_exp_f32_e32 v195, v195
	v_exp_f32_e32 v196, v196
	v_exp_f32_e32 v197, v197
	v_exp_f32_e32 v198, v198
	v_exp_f32_e32 v199, v199
	v_add_f32_e32 v192, 1.0, v192
	v_add_f32_e32 v193, 1.0, v193
	v_add_f32_e32 v194, 1.0, v194
	v_add_f32_e32 v195, 1.0, v195
	v_add_f32_e32 v196, 1.0, v196
	v_add_f32_e32 v197, 1.0, v197
	v_add_f32_e32 v198, 1.0, v198
	v_add_f32_e32 v199, 1.0, v199
	v_rcp_f32_e32 v192, v192
	v_rcp_f32_e32 v193, v193
	v_rcp_f32_e32 v194, v194
	v_rcp_f32_e32 v195, v195
	v_rcp_f32_e32 v196, v196
	v_rcp_f32_e32 v197, v197
	v_rcp_f32_e32 v198, v198
	v_rcp_f32_e32 v199, v199
	v_pk_mul_f32 v[192:193], v[42:43], v[192:193]
	v_pk_mul_f32 v[194:195], v[44:45], v[194:195]
	v_pk_mul_f32 v[196:197], v[46:47], v[196:197]
	v_pk_mul_f32 v[198:199], v[48:49], v[198:199]
	v_pk_mul_f32 v[202:203], v[192:193], v[34:35]
	v_pk_mul_f32 v[204:205], v[194:195], v[36:37]
	v_pk_mul_f32 v[206:207], v[196:197], v[38:39]
	v_pk_mul_f32 v[208:209], v[198:199], v[40:41]
	v_cvt_pk_bf16_f32 v210, v206, v207
	v_cvt_pk_bf16_f32 v211, v208, v209
	v_cvt_pk_bf16_f32 v212, v202, v203
	v_cvt_pk_bf16_f32 v213, v204, v205
	global_store_dwordx4 v[218:219], v[210:213], off
	v_add_co_u32_e32 v218, vcc, 0x16000, v218
	s_nop 1
	v_addc_co_u32_e32 v219, vcc, 0, v219, vcc
	v_pk_fma_f32 v[30:31], v[30:31], v[188:189], v[78:79] op_sel_hi:[1,0,1]
	v_pk_fma_f32 v[32:33], v[32:33], v[188:189], v[80:81] op_sel_hi:[1,0,1]
	v_pk_fma_f32 v[26:27], v[26:27], v[188:189], v[74:75] op_sel_hi:[1,0,1]
	v_pk_fma_f32 v[28:29], v[28:29], v[188:189], v[76:77] op_sel_hi:[1,0,1]
	v_pk_fma_f32 v[22:23], v[22:23], v[188:189], v[62:63] op_sel_hi:[1,0,1]
	v_pk_fma_f32 v[24:25], v[24:25], v[188:189], v[64:65] op_sel_hi:[1,0,1]
	v_pk_fma_f32 v[18:19], v[18:19], v[188:189], v[58:59] op_sel_hi:[1,0,1]
	v_pk_fma_f32 v[20:21], v[20:21], v[188:189], v[60:61] op_sel_hi:[1,0,1]
	v_pk_mul_f32 v[192:193], v[26:27], s[26:27] op_sel_hi:[1,0]
	v_pk_mul_f32 v[194:195], v[28:29], s[26:27] op_sel_hi:[1,0]
	v_pk_mul_f32 v[196:197], v[30:31], s[26:27] op_sel_hi:[1,0]
	v_pk_mul_f32 v[198:199], v[32:33], s[26:27] op_sel_hi:[1,0]
	v_exp_f32_e32 v192, v192
	v_exp_f32_e32 v193, v193
	v_exp_f32_e32 v194, v194
	v_exp_f32_e32 v195, v195
	v_exp_f32_e32 v196, v196
	v_exp_f32_e32 v197, v197
	v_exp_f32_e32 v198, v198
	v_exp_f32_e32 v199, v199
	v_add_f32_e32 v192, 1.0, v192
	v_add_f32_e32 v193, 1.0, v193
	v_add_f32_e32 v194, 1.0, v194
	v_add_f32_e32 v195, 1.0, v195
	v_add_f32_e32 v196, 1.0, v196
	v_add_f32_e32 v197, 1.0, v197
	v_add_f32_e32 v198, 1.0, v198
	v_add_f32_e32 v199, 1.0, v199
	v_rcp_f32_e32 v192, v192
	v_rcp_f32_e32 v193, v193
	v_rcp_f32_e32 v194, v194
	v_rcp_f32_e32 v195, v195
	v_rcp_f32_e32 v196, v196
	v_rcp_f32_e32 v197, v197
	v_rcp_f32_e32 v198, v198
	v_rcp_f32_e32 v199, v199
	v_pk_mul_f32 v[192:193], v[26:27], v[192:193]
	v_pk_mul_f32 v[194:195], v[28:29], v[194:195]
	v_pk_mul_f32 v[196:197], v[30:31], v[196:197]
	v_pk_mul_f32 v[198:199], v[32:33], v[198:199]
	v_pk_mul_f32 v[202:203], v[192:193], v[18:19]
	v_pk_mul_f32 v[204:205], v[194:195], v[20:21]
	v_pk_mul_f32 v[206:207], v[196:197], v[22:23]
	v_pk_mul_f32 v[208:209], v[198:199], v[24:25]
	v_cvt_pk_bf16_f32 v210, v206, v207
	v_cvt_pk_bf16_f32 v211, v208, v209
	v_cvt_pk_bf16_f32 v212, v202, v203
	v_cvt_pk_bf16_f32 v213, v204, v205
	global_store_dwordx4 v[218:219], v[210:213], off
	v_add_co_u32_e32 v218, vcc, 0x16000, v218
	s_nop 1
	v_addc_co_u32_e32 v219, vcc, 0, v219, vcc
	v_pk_fma_f32 v[14:15], v[14:15], v[190:191], v[78:79] op_sel_hi:[1,0,1]
	v_pk_fma_f32 v[16:17], v[16:17], v[190:191], v[80:81] op_sel_hi:[1,0,1]
	v_pk_fma_f32 v[10:11], v[10:11], v[190:191], v[74:75] op_sel_hi:[1,0,1]
	v_pk_fma_f32 v[12:13], v[12:13], v[190:191], v[76:77] op_sel_hi:[1,0,1]
	v_pk_fma_f32 v[6:7], v[6:7], v[190:191], v[62:63] op_sel_hi:[1,0,1]
	v_pk_fma_f32 v[8:9], v[8:9], v[190:191], v[64:65] op_sel_hi:[1,0,1]
	v_pk_fma_f32 v[2:3], v[2:3], v[190:191], v[58:59] op_sel_hi:[1,0,1]
	v_pk_fma_f32 v[4:5], v[4:5], v[190:191], v[60:61] op_sel_hi:[1,0,1]
	v_pk_mul_f32 v[192:193], v[10:11], s[26:27] op_sel_hi:[1,0]
	v_pk_mul_f32 v[194:195], v[12:13], s[26:27] op_sel_hi:[1,0]
	v_pk_mul_f32 v[196:197], v[14:15], s[26:27] op_sel_hi:[1,0]
	v_pk_mul_f32 v[198:199], v[16:17], s[26:27] op_sel_hi:[1,0]
	v_exp_f32_e32 v192, v192
	v_exp_f32_e32 v193, v193
	v_exp_f32_e32 v194, v194
	v_exp_f32_e32 v195, v195
	v_exp_f32_e32 v196, v196
	v_exp_f32_e32 v197, v197
	v_exp_f32_e32 v198, v198
	v_exp_f32_e32 v199, v199
	v_add_f32_e32 v192, 1.0, v192
	v_add_f32_e32 v193, 1.0, v193
	v_add_f32_e32 v194, 1.0, v194
	v_add_f32_e32 v195, 1.0, v195
	v_add_f32_e32 v196, 1.0, v196
	v_add_f32_e32 v197, 1.0, v197
	v_add_f32_e32 v198, 1.0, v198
	v_add_f32_e32 v199, 1.0, v199
	v_rcp_f32_e32 v192, v192
	v_rcp_f32_e32 v193, v193
	v_rcp_f32_e32 v194, v194
	v_rcp_f32_e32 v195, v195
	v_rcp_f32_e32 v196, v196
	v_rcp_f32_e32 v197, v197
	v_rcp_f32_e32 v198, v198
	v_rcp_f32_e32 v199, v199
	v_pk_mul_f32 v[192:193], v[10:11], v[192:193]
	v_pk_mul_f32 v[194:195], v[12:13], v[194:195]
	v_pk_mul_f32 v[196:197], v[14:15], v[196:197]
	v_pk_mul_f32 v[198:199], v[16:17], v[198:199]
	v_pk_mul_f32 v[202:203], v[192:193], v[2:3]
	v_pk_mul_f32 v[204:205], v[194:195], v[4:5]
	v_pk_mul_f32 v[206:207], v[196:197], v[6:7]
	v_pk_mul_f32 v[208:209], v[198:199], v[8:9]
	v_cvt_pk_bf16_f32 v210, v206, v207
	v_cvt_pk_bf16_f32 v211, v208, v209
	v_cvt_pk_bf16_f32 v212, v202, v203
	v_cvt_pk_bf16_f32 v213, v204, v205
	global_store_dwordx4 v[218:219], v[210:213], off
	s_andn2_b64 vcc, exec, s[4:5]
	s_mov_b64 s[4:5], -1
	s_branch .Lp8_tail
